# v15 + down-projection scale bytes collected in LDS over 4 flushes and stored as 64-byte pieces (2 per row per tile instead of 8 x 16 B)
# baseline (speedup 1.0000x reference)
; DI void phase_edown3(const Ctx& c, int layer) {
;     ...
;         D2_BODY(0, 0, 0); D2_BODY(1, 1, 0);
; #pragma unroll 1
;         for (int J = 2; J < 16; J += 2) { D2_BODY(0, J, 5); D2_BODY(1, J + 1, 0); }
.Ledc_dn3:
	s_and_saveexec_b64 s[6:7], s[4:5]
	s_xor_b64 s[6:7], exec, s[6:7]
	v_mad_i64_i32 v[72:73], s[8:9], v78, s50, 0
	s_andn2_saveexec_b64 s[6:7], s[6:7]
	s_cbranch_execz .LBB0_1286
	ds_read_b128 v[80:83], v104 offset:128
	v_mov_b64_e32 v[84:85], s[10:11]
	v_mad_i64_i32 v[72:73], s[8:9], v78, s50, 0
	v_mad_i64_i32 v[78:79], s[8:9], v78, s50, v[84:85]
	s_waitcnt lgkmcnt(0)
	v_readlane_b32 s44, v255, 3
	s_lshl_b32 s44, s44, 11
	s_add_i32 s44, s44, 0x1a000
	v_mbcnt_lo_u32_b32 v196, -1, 0
	v_mbcnt_hi_u32_b32 v196, -1, v196
	v_lshl_add_u32 v197, v196, 6, s44
	ds_write_b128 v197, v[80:83]
.LBB0_1286:
	s_or_b64 exec, exec, s[6:7]
	s_nop 0
	v_mad_i64_i32 v[80:81], s[6:7], v74, s50, 0
	v_mad_i64_i32 v[78:79], s[6:7], v75, s50, 0
	v_mad_i64_i32 v[82:83], s[6:7], v76, s50, 0
	v_mad_i64_i32 v[74:75], s[6:7], v77, s50, 0
	s_mov_b64 s[6:7], 0x2e2c2c10
	s_nop 0
	v_lshl_add_u64 v[72:73], v[72:73], 0, s[6:7]
	v_lshl_add_u64 v[74:75], v[70:71], 0, v[74:75]
	v_lshl_add_u64 v[76:77], v[70:71], 0, v[82:83]
	v_lshl_add_u64 v[78:79], v[70:71], 0, v[78:79]
	v_lshl_add_u64 v[80:81], v[70:71], 0, v[80:81]
	s_mov_b32 s43, s40
	s_mov_b32 s40, 2
	s_branch .LBB0_1288
.LBB0_1287:
	s_or_b64 exec, exec, s[8:9]
	s_and_b32 s45, s40, 6
	s_cmp_lg_u32 s45, 6
	s_cbranch_scc1 .Lsc_skip
	v_readlane_b32 s44, v255, 3
	s_lshl_b32 s46, s44, 5
	s_lshl_b32 s44, s44, 11
	s_add_i32 s44, s44, 0x1a000
	v_mbcnt_lo_u32_b32 v196, -1, 0
	v_mbcnt_hi_u32_b32 v196, -1, v196
	v_lshl_add_u32 v197, v196, 4, s44
	s_waitcnt lgkmcnt(0)
	ds_read_b128 v[198:201], v197
	ds_read_b128 v[202:205], v197 offset:1024
	s_add_i32 s46, s46, s43
	v_lshrrev_b32_e32 v206, 2, v196
	v_add_u32_e32 v206, s46, v206
	v_and_b32_e32 v207, 3, v196
	v_lshlrev_b32_e32 v207, 4, v207
	s_and_b32 s45, s40, 8
	s_lshl_b32 s45, s45, 3
	s_addk_i32 s45, 0x400
	v_add_u32_e32 v207, s45, v207
	v_mad_u32_u24 v208, v206, s50, v207
	v_add_u32_e32 v209, 0x4800, v208
	s_waitcnt lgkmcnt(0)
	s_cmp_lt_u32 s28, 2
	s_cbranch_scc1 .Lsc_nt
	global_store_dwordx4 v208, v[198:201], s[10:11]
	global_store_dwordx4 v209, v[202:205], s[10:11]
	s_branch .Lsc_skip
.Lsc_nt:
	global_store_dwordx4 v208, v[198:201], s[10:11] nt
	global_store_dwordx4 v209, v[202:205], s[10:11] nt
.Lsc_skip:
	s_add_i32 s40, s40, 2
	s_add_u32 s16, s16, 0x10000
	v_lshl_add_u64 v[72:73], v[72:73], 0, 16
	v_lshl_add_u64 v[74:75], v[74:75], 0, s[70:71]
	v_lshl_add_u64 v[76:77], v[76:77], 0, s[70:71]
	v_lshl_add_u64 v[78:79], v[78:79], 0, s[70:71]
	v_lshl_add_u64 v[80:81], v[80:81], 0, s[70:71]
	s_addc_u32 s17, s17, 0
	s_and_b64 vcc, exec, s[6:7]
	s_cbranch_vccnz .LBB0_1256
.LBB0_1288:
	v_lshl_add_u64 v[82:83], s[16:17], 0, v[176:177]
	s_mov_b32 m0, s36
	v_lshl_add_u64 v[84:85], v[82:83], 0, s[80:81]
	s_waitcnt vmcnt(4)
	s_barrier
	global_load_lds_dwordx4 v[84:85], off
	v_lshl_add_u64 v[84:85], s[16:17], 0, v[64:65]
	v_lshl_add_u64 v[110:111], v[84:85], 0, s[80:81]
	s_mov_b32 m0, s37
	s_nop 0
	global_load_lds_dwordx4 v[110:111], off
	v_lshl_add_u64 v[110:111], v[82:83], 0, s[82:83]
	s_mov_b32 m0, s38
	s_nop 0
	global_load_lds_dwordx4 v[110:111], off
	v_lshl_add_u64 v[110:111], v[84:85], 0, s[82:83]
	s_mov_b32 m0, s39
	s_nop 0
	global_load_lds_dwordx4 v[110:111], off
	ds_read_b128 v[110:113], v94
	ds_read_b128 v[114:117], v94 offset:8192
	ds_read_b128 v[118:121], v95
	ds_read_b128 v[122:125], v95 offset:8192
	ds_read_b128 v[126:129], v96
	ds_read_b128 v[130:133], v96 offset:8192
	ds_read_b128 v[134:137], v97
	ds_read_b128 v[138:141], v97 offset:8192
	ds_read_b128 v[142:145], v98
	ds_read_b128 v[146:149], v98 offset:8192
	ds_read_b128 v[150:153], v99
	ds_read_b128 v[154:157], v99 offset:8192
	ds_read_b128 v[158:161], v100
	ds_read_b128 v[162:165], v100 offset:8192
	ds_read_b128 v[166:169], v101
	ds_read_b128 v[170:173], v101 offset:8192
	s_setprio 1
	s_waitcnt lgkmcnt(0)
	v_mfma_f32_16x16x32_bf16 v[178:181], v[110:113], v[0:3], 0
	v_mfma_f32_16x16x32_bf16 v[182:185], v[114:117], v[0:3], 0
	v_mfma_f32_16x16x32_bf16 v[110:113], v[110:113], v[32:35], 0
	v_mfma_f32_16x16x32_bf16 v[114:117], v[114:117], v[32:35], 0
	v_mfma_f32_16x16x32_bf16 v[178:181], v[118:121], v[4:7], v[178:181]
	v_mfma_f32_16x16x32_bf16 v[182:185], v[122:125], v[4:7], v[182:185]
	v_mfma_f32_16x16x32_bf16 v[110:113], v[118:121], v[36:39], v[110:113]
	v_mfma_f32_16x16x32_bf16 v[114:117], v[122:125], v[36:39], v[114:117]
	v_mfma_f32_16x16x32_bf16 v[118:121], v[126:129], v[8:11], v[178:181]
	v_mfma_f32_16x16x32_bf16 v[122:125], v[130:133], v[8:11], v[182:185]
	v_mfma_f32_16x16x32_bf16 v[110:113], v[126:129], v[40:43], v[110:113]
	v_mfma_f32_16x16x32_bf16 v[114:117], v[130:133], v[40:43], v[114:117]
	v_mfma_f32_16x16x32_bf16 v[118:121], v[134:137], v[12:15], v[118:121]
	v_mfma_f32_16x16x32_bf16 v[122:125], v[138:141], v[12:15], v[122:125]
	v_mfma_f32_16x16x32_bf16 v[110:113], v[134:137], v[44:47], v[110:113]
	v_mfma_f32_16x16x32_bf16 v[114:117], v[138:141], v[44:47], v[114:117]
	v_mfma_f32_16x16x32_bf16 v[118:121], v[142:145], v[16:19], v[118:121]
	v_mfma_f32_16x16x32_bf16 v[122:125], v[146:149], v[16:19], v[122:125]
	v_mfma_f32_16x16x32_bf16 v[110:113], v[142:145], v[48:51], v[110:113]
	v_mfma_f32_16x16x32_bf16 v[114:117], v[146:149], v[48:51], v[114:117]
	v_mfma_f32_16x16x32_bf16 v[118:121], v[150:153], v[20:23], v[118:121]
	v_mfma_f32_16x16x32_bf16 v[122:125], v[154:157], v[20:23], v[122:125]
	v_mfma_f32_16x16x32_bf16 v[110:113], v[150:153], v[52:55], v[110:113]
	v_mfma_f32_16x16x32_bf16 v[114:117], v[154:157], v[52:55], v[114:117]
	v_mfma_f32_16x16x32_bf16 v[118:121], v[158:161], v[24:27], v[118:121]
	v_mfma_f32_16x16x32_bf16 v[122:125], v[162:165], v[24:27], v[122:125]
	v_mfma_f32_16x16x32_bf16 v[110:113], v[158:161], v[56:59], v[110:113]
	v_mfma_f32_16x16x32_bf16 v[114:117], v[162:165], v[56:59], v[114:117]
	v_mfma_f32_16x16x32_bf16 v[118:121], v[166:169], v[28:31], v[118:121]
	v_mfma_f32_16x16x32_bf16 v[122:125], v[170:173], v[28:31], v[122:125]
	v_mfma_f32_16x16x32_bf16 v[110:113], v[166:169], v[60:63], v[110:113]
	v_mfma_f32_16x16x32_bf16 v[114:117], v[170:173], v[60:63], v[114:117]
	s_setprio 0
	s_nop 3
	v_max_f32_e64 v174, |v119|, |v119|
	v_max_f32_e64 v175, |v118|, |v118|
	v_max_f32_e32 v174, v175, v174
	v_max_f32_e64 v175, |v121|, |v121|
	v_max_f32_e64 v194, |v120|, |v120|
	v_max_f32_e32 v175, v194, v175
	v_max_f32_e64 v194, |v125|, |v125|
	v_max_f32_e64 v195, |v124|, |v124|
	v_max_f32_e32 v194, v195, v194
	v_max3_f32 v194, |v122|, |v123|, v194
	v_max3_f32 v174, v174, v175, v194
	v_mul_f32_e32 v174, 0x3c010204, v174
	v_lshrrev_b32_e32 v175, 23, v174
	v_and_b32_e32 v174, 0x7f800000, v174
	v_sub_u32_e32 v174, 0x7e800000, v174
	v_fmaak_f32 v118, v118, v174, 0x43000000
	v_cvt_pk_u8_f32 v118, v118, 0, 0
	v_fmaak_f32 v119, v119, v174, 0x43000000
	v_cvt_pk_u8_f32 v118, v119, 1, v118
	v_fmaak_f32 v119, v120, v174, 0x43000000
	v_cvt_pk_u8_f32 v118, v119, 2, v118
	v_fmaak_f32 v119, v121, v174, 0x43000000
	v_cvt_pk_u8_f32 v118, v119, 3, v118
	v_fmaak_f32 v119, v122, v174, 0x43000000
	v_cvt_pk_u8_f32 v119, v119, 0, 0
	v_fmaak_f32 v120, v123, v174, 0x43000000
	v_cvt_pk_u8_f32 v119, v120, 1, v119
	v_fmaak_f32 v120, v124, v174, 0x43000000
	v_cvt_pk_u8_f32 v119, v120, 2, v119
	v_fmaak_f32 v120, v125, v174, 0x43000000
	v_cvt_pk_u8_f32 v119, v120, 3, v119
	v_add_u16_e32 v120, 1, v175
	ds_read_b128 v[126:129], v94 offset:16384
	ds_read_b128 v[130:133], v94 offset:24576
	ds_read_b128 v[134:137], v95 offset:16384
	ds_read_b128 v[138:141], v95 offset:24576
	ds_read_b128 v[142:145], v96 offset:16384
	ds_read_b128 v[146:149], v96 offset:24576
	ds_read_b128 v[150:153], v97 offset:16384
	ds_read_b128 v[154:157], v97 offset:24576
	ds_read_b128 v[158:161], v98 offset:16384
	ds_read_b128 v[162:165], v98 offset:24576
	ds_read_b128 v[166:169], v99 offset:16384
	ds_read_b128 v[170:173], v99 offset:24576
	ds_read_b128 v[178:181], v100 offset:16384
	ds_read_b128 v[182:185], v100 offset:24576
	ds_read_b128 v[186:189], v101 offset:16384
	ds_read_b128 v[190:193], v101 offset:24576
	ds_write_b8 v106, v120 offset:128
	v_max_f32_e64 v120, |v111|, |v111|
	v_max_f32_e64 v121, |v110|, |v110|
	v_max_f32_e32 v120, v121, v120
	v_max_f32_e64 v121, |v113|, |v113|
	v_max_f32_e64 v122, |v112|, |v112|
	v_max_f32_e32 v121, v122, v121
	v_max_f32_e64 v122, |v117|, |v117|
	v_max_f32_e64 v123, |v116|, |v116|
	v_max_f32_e32 v122, v123, v122
	v_max3_f32 v122, |v114|, |v115|, v122
	v_max3_f32 v120, v120, v121, v122
	v_mul_f32_e32 v120, 0x3c010204, v120
	v_lshrrev_b32_e32 v121, 23, v120
	v_and_b32_e32 v120, 0x7f800000, v120
	v_sub_u32_e32 v120, 0x7e800000, v120
	v_fmaak_f32 v110, v110, v120, 0x43000000
	v_cvt_pk_u8_f32 v110, v110, 0, 0
	v_fmaak_f32 v111, v111, v120, 0x43000000
	v_cvt_pk_u8_f32 v110, v111, 1, v110
	v_fmaak_f32 v111, v112, v120, 0x43000000
	v_cvt_pk_u8_f32 v110, v111, 2, v110
	v_fmaak_f32 v111, v113, v120, 0x43000000
	v_cvt_pk_u8_f32 v110, v111, 3, v110
	v_fmaak_f32 v111, v114, v120, 0x43000000
	v_cvt_pk_u8_f32 v111, v111, 0, 0
	v_fmaak_f32 v112, v115, v120, 0x43000000
	v_cvt_pk_u8_f32 v111, v112, 1, v111
	v_fmaak_f32 v112, v116, v120, 0x43000000
	v_cvt_pk_u8_f32 v111, v112, 2, v111
	v_fmaak_f32 v112, v117, v120, 0x43000000
	v_cvt_pk_u8_f32 v111, v112, 3, v111
	ds_write2st64_b64 v102, v[118:119], v[110:111] offset1:5
	v_add_u16_e32 v110, 1, v121
	ds_write_b8 v106, v110 offset:2688
	s_setprio 1
	s_waitcnt lgkmcnt(0)
	v_mfma_f32_16x16x32_bf16 v[110:113], v[126:129], v[0:3], 0
	v_mfma_f32_16x16x32_bf16 v[114:117], v[130:133], v[0:3], 0
	v_mfma_f32_16x16x32_bf16 v[118:121], v[126:129], v[32:35], 0
	v_mfma_f32_16x16x32_bf16 v[122:125], v[130:133], v[32:35], 0
	v_mfma_f32_16x16x32_bf16 v[110:113], v[134:137], v[4:7], v[110:113]
	v_mfma_f32_16x16x32_bf16 v[114:117], v[138:141], v[4:7], v[114:117]
	v_mfma_f32_16x16x32_bf16 v[118:121], v[134:137], v[36:39], v[118:121]
	v_mfma_f32_16x16x32_bf16 v[122:125], v[138:141], v[36:39], v[122:125]
	v_mfma_f32_16x16x32_bf16 v[110:113], v[142:145], v[8:11], v[110:113]
	v_mfma_f32_16x16x32_bf16 v[114:117], v[146:149], v[8:11], v[114:117]
	v_mfma_f32_16x16x32_bf16 v[118:121], v[142:145], v[40:43], v[118:121]
	v_mfma_f32_16x16x32_bf16 v[122:125], v[146:149], v[40:43], v[122:125]
	v_mfma_f32_16x16x32_bf16 v[110:113], v[150:153], v[12:15], v[110:113]
	v_mfma_f32_16x16x32_bf16 v[114:117], v[154:157], v[12:15], v[114:117]
	v_mfma_f32_16x16x32_bf16 v[118:121], v[150:153], v[44:47], v[118:121]
	v_mfma_f32_16x16x32_bf16 v[122:125], v[154:157], v[44:47], v[122:125]
	v_mfma_f32_16x16x32_bf16 v[110:113], v[158:161], v[16:19], v[110:113]
	v_mfma_f32_16x16x32_bf16 v[114:117], v[162:165], v[16:19], v[114:117]
	v_mfma_f32_16x16x32_bf16 v[118:121], v[158:161], v[48:51], v[118:121]
	v_mfma_f32_16x16x32_bf16 v[122:125], v[162:165], v[48:51], v[122:125]
	v_mfma_f32_16x16x32_bf16 v[110:113], v[166:169], v[20:23], v[110:113]
	v_mfma_f32_16x16x32_bf16 v[114:117], v[170:173], v[20:23], v[114:117]
	v_mfma_f32_16x16x32_bf16 v[118:121], v[166:169], v[52:55], v[118:121]
	v_mfma_f32_16x16x32_bf16 v[122:125], v[170:173], v[52:55], v[122:125]
	v_mfma_f32_16x16x32_bf16 v[110:113], v[178:181], v[24:27], v[110:113]
	v_mfma_f32_16x16x32_bf16 v[114:117], v[182:185], v[24:27], v[114:117]
	v_mfma_f32_16x16x32_bf16 v[118:121], v[178:181], v[56:59], v[118:121]
	v_mfma_f32_16x16x32_bf16 v[122:125], v[182:185], v[56:59], v[122:125]
	v_mfma_f32_16x16x32_bf16 v[110:113], v[186:189], v[28:31], v[110:113]
	v_mfma_f32_16x16x32_bf16 v[114:117], v[190:193], v[28:31], v[114:117]
	v_mfma_f32_16x16x32_bf16 v[118:121], v[186:189], v[60:63], v[118:121]
	v_mfma_f32_16x16x32_bf16 v[122:125], v[190:193], v[60:63], v[122:125]
	s_setprio 0
	s_nop 3
	v_max_f32_e64 v126, |v111|, |v111|
	v_max_f32_e64 v127, |v110|, |v110|
	v_max_f32_e32 v126, v127, v126
	v_max_f32_e64 v127, |v113|, |v113|
	v_max_f32_e64 v128, |v112|, |v112|
	v_max_f32_e32 v127, v128, v127
	v_max_f32_e64 v128, |v117|, |v117|
	v_max_f32_e64 v129, |v116|, |v116|
	v_max_f32_e32 v128, v129, v128
	v_max3_f32 v128, |v114|, |v115|, v128
	v_max3_f32 v126, v126, v127, v128
	v_mul_f32_e32 v126, 0x3c010204, v126
	v_lshrrev_b32_e32 v127, 23, v126
	v_and_b32_e32 v126, 0x7f800000, v126
	v_sub_u32_e32 v126, 0x7e800000, v126
	v_fmaak_f32 v110, v110, v126, 0x43000000
	v_cvt_pk_u8_f32 v110, v110, 0, 0
	v_fmaak_f32 v111, v111, v126, 0x43000000
	v_cvt_pk_u8_f32 v110, v111, 1, v110
	v_fmaak_f32 v111, v112, v126, 0x43000000
	v_cvt_pk_u8_f32 v110, v111, 2, v110
	v_fmaak_f32 v111, v113, v126, 0x43000000
	v_cvt_pk_u8_f32 v110, v111, 3, v110
	v_fmaak_f32 v111, v114, v126, 0x43000000
	v_cvt_pk_u8_f32 v111, v111, 0, 0
	v_fmaak_f32 v112, v115, v126, 0x43000000
	v_cvt_pk_u8_f32 v111, v112, 1, v111
	v_fmaak_f32 v112, v116, v126, 0x43000000
	v_cvt_pk_u8_f32 v111, v112, 2, v111
	v_fmaak_f32 v112, v117, v126, 0x43000000
	v_cvt_pk_u8_f32 v111, v112, 3, v111
	v_add_u16_e32 v112, 1, v127
	ds_write_b8 v106, v112 offset:132
	v_max_f32_e64 v112, |v119|, |v119|
	v_max_f32_e64 v113, |v118|, |v118|
	v_max_f32_e32 v112, v113, v112
	v_max_f32_e64 v113, |v121|, |v121|
	v_max_f32_e64 v114, |v120|, |v120|
	v_max_f32_e32 v113, v114, v113
	v_max_f32_e64 v114, |v125|, |v125|
	v_max_f32_e64 v115, |v124|, |v124|
	v_max_f32_e32 v114, v115, v114
	v_max3_f32 v114, |v122|, |v123|, v114
	v_max3_f32 v112, v112, v113, v114
	v_mul_f32_e32 v112, 0x3c010204, v112
	v_lshrrev_b32_e32 v114, 23, v112
	v_and_b32_e32 v112, 0x7f800000, v112
	v_sub_u32_e32 v113, 0x7e800000, v112
	v_fmaak_f32 v112, v118, v113, 0x43000000
	v_cvt_pk_u8_f32 v112, v112, 0, 0
	v_fmaak_f32 v115, v119, v113, 0x43000000
	v_cvt_pk_u8_f32 v112, v115, 1, v112
	v_fmaak_f32 v115, v120, v113, 0x43000000
	v_cvt_pk_u8_f32 v112, v115, 2, v112
	v_fmaak_f32 v115, v121, v113, 0x43000000
	v_cvt_pk_u8_f32 v112, v115, 3, v112
	v_fmaak_f32 v115, v122, v113, 0x43000000
	v_cvt_pk_u8_f32 v115, v115, 0, 0
	v_fmaak_f32 v116, v123, v113, 0x43000000
	v_cvt_pk_u8_f32 v115, v116, 1, v115
	v_fmaak_f32 v116, v124, v113, 0x43000000
	v_cvt_pk_u8_f32 v115, v116, 2, v115
	v_fmaak_f32 v113, v125, v113, 0x43000000
	v_cvt_pk_u8_f32 v113, v113, 3, v115
	ds_write2st64_b64 v107, v[110:111], v[112:113] offset1:5
	v_add_u16_e32 v110, 1, v114
	ds_write_b8 v106, v110 offset:2692
	s_waitcnt vmcnt(0)
	s_cmp_gt_u32 s40, 13
	s_cselect_b64 s[6:7], -1, 0
	s_and_b64 vcc, exec, s[6:7]
	s_barrier
	s_cbranch_vccnz .LBB0_1290
	s_mov_b32 m0, s30
	v_lshl_add_u64 v[110:111], v[82:83], 0, s[78:79]
	v_lshl_add_u64 v[112:113], v[84:85], 0, s[78:79]
	global_load_lds_dwordx4 v[110:111], off
	s_mov_b32 m0, s18
	v_lshl_add_u64 v[82:83], v[82:83], 0, s[84:85]
	global_load_lds_dwordx4 v[112:113], off
	s_mov_b32 m0, s19
	v_lshl_add_u64 v[84:85], v[84:85], 0, s[84:85]
	global_load_lds_dwordx4 v[82:83], off
	s_mov_b32 m0, s31
	s_nop 0
	global_load_lds_dwordx4 v[84:85], off

.Ledc_dn8:
	s_and_saveexec_b64 s[8:9], s[2:3]
	s_cbranch_execz .LBB0_1287
	ds_read_b128 v[82:85], v104 offset:128
	v_lshl_add_u64 v[110:111], s[0:1], 0, v[72:73]
	s_waitcnt lgkmcnt(0)
	v_readlane_b32 s44, v255, 3
	s_lshl_b32 s44, s44, 11
	s_add_i32 s44, s44, 0x1a000
	s_and_b32 s45, s40, 6
	s_lshl_b32 s45, s45, 3
	s_add_i32 s44, s44, s45
	v_mbcnt_lo_u32_b32 v196, -1, 0
	v_mbcnt_hi_u32_b32 v196, -1, v196
	v_lshl_add_u32 v197, v196, 6, s44
	ds_write_b128 v197, v[82:85]
	s_branch .LBB0_1287
